# speedup vs baseline: 1.0300x; 1.0300x over previous
_Z9ssim_mainPKfS0_S0_Pf:
	v_readfirstlane_b32 s29, v0
	s_load_dwordx4 s[4:7], s[0:1], 0x0
	s_load_dwordx4 s[8:11], s[0:1], 0x10
	s_mov_b32 s51, 0x44800000
	s_mov_b32 s38, 0
	s_mov_b32 s39, -1
	s_lshr_b32 s12, s29, 6
	s_and_b32 s13, s2, 7
	s_lshl_b32 s13, s13, 5
	s_lshr_b32 s14, s2, 3
	s_add_u32 s13, s13, s14
	s_lshr_b32 s14, s13, 3
	s_and_b32 s15, s13, 7
	s_lshl_b32 s16, s14, 20
	s_lshl_b32 s17, s15, 17
	s_add_u32 s16, s16, s17
	s_lshl_b32 s17, s12, 8
	s_add_u32 s16, s16, s17
	s_lshl_b32 s27, s12, 2
	s_add_u32 s27, s27, 0x10000
	v_and_b32_e32 v8, 63, v0
	v_and_b32_e32 v169, 15, v0
	v_bfe_u32 v164, v0, 4, 2
	v_lshrrev_b32_e32 v167, 2, v169
	v_lshlrev_b32_e32 v167, 5, v167
	v_and_b32_e32 v168, 1, v169
	v_lshl_or_b32 v167, v168, 4, v167
	v_bfe_u32 v168, v169, 1, 1
	v_lshl_or_b32 v167, v168, 7, v167
	v_lshl_or_b32 v9, v164, 14, v167
	v_and_b32_e32 v168, 1, v164
	v_lshl_or_b32 v23, v168, 14, v167
	v_lshrrev_b32_e32 v168, 1, v164
	v_lshl_or_b32 v23, v168, 13, v23
	v_add_u32_e32 v237, 0x1000, v9
	v_add_u32_e32 v238, 0x2000, v9
	v_add_u32_e32 v239, 0x3000, v9
	v_add_u32_e32 v240, 0x10000, v9
	v_add_u32_e32 v241, 0x11000, v9
	v_add_u32_e32 v242, 0x12000, v9
	v_add_u32_e32 v243, 0x13000, v9
	s_waitcnt lgkmcnt(0)
	s_load_dwordx8 s[40:47], s[8:9], 0x0
	s_load_dwordx2 s[48:49], s[8:9], 0x20
	s_load_dword s50, s[8:9], 0x28
	s_add_u32 s18, s4, s16
	s_addc_u32 s19, s5, 0
	s_add_u32 s20, s6, s16
	s_addc_u32 s21, s7, 0
	global_load_dwordx4 v[36:39], v9, s[18:19] offset:0 sc1 nt
	global_load_dwordx4 v[40:43], v9, s[18:19] offset:2048 sc1 nt
	global_load_dwordx4 v[68:71], v9, s[20:21] offset:0 sc1 nt
	global_load_dwordx4 v[72:75], v9, s[20:21] offset:2048 sc1 nt
	global_load_dwordx4 v[44:47], v237, s[18:19] offset:0 sc1 nt
	global_load_dwordx4 v[48:51], v237, s[18:19] offset:2048 sc1 nt
	global_load_dwordx4 v[76:79], v237, s[20:21] offset:0 sc1 nt
	global_load_dwordx4 v[80:83], v237, s[20:21] offset:2048 sc1 nt
	global_load_dwordx4 v[52:55], v238, s[18:19] offset:0 sc1 nt
	global_load_dwordx4 v[56:59], v238, s[18:19] offset:2048 sc1 nt
	global_load_dwordx4 v[84:87], v238, s[20:21] offset:0 sc1 nt
	global_load_dwordx4 v[88:91], v238, s[20:21] offset:2048 sc1 nt
	global_load_dwordx4 v[60:63], v239, s[18:19] offset:0 sc1 nt
	global_load_dwordx4 v[64:67], v239, s[18:19] offset:2048 sc1 nt
	global_load_dwordx4 v[92:95], v239, s[20:21] offset:0 sc1 nt
	global_load_dwordx4 v[96:99], v239, s[20:21] offset:2048 sc1 nt
	v_mov_b32_e32 v6, s27
	v_mov_b32_e32 v168, 0
	ds_write_b32 v6, v168 offset:0
	ds_write_b32 v6, v168 offset:32
	ds_write_b32 v6, v168 offset:64
	ds_write_b32 v6, v168 offset:96
	v_lshlrev_b32_e32 v167, 3, v164
	v_xor_b32_e32 v168, 16, v167
	v_sub_u32_e32 v165, v167, v169
	v_sub_u32_e32 v166, v168, v169
	v_add_u32_e32 v172, 0, v165
	v_min_u32_e32 v172, 11, v172
	v_lshlrev_b32_e32 v172, 2, v172
	v_add_u32_e32 v173, 1, v165
	v_min_u32_e32 v173, 11, v173
	v_lshlrev_b32_e32 v173, 2, v173
	v_add_u32_e32 v174, 2, v165
	v_min_u32_e32 v174, 11, v174
	v_lshlrev_b32_e32 v174, 2, v174
	v_add_u32_e32 v175, 3, v165
	v_min_u32_e32 v175, 11, v175
	v_lshlrev_b32_e32 v175, 2, v175
	v_add_u32_e32 v176, 4, v165
	v_min_u32_e32 v176, 11, v176
	v_lshlrev_b32_e32 v176, 2, v176
	v_add_u32_e32 v177, 5, v165
	v_min_u32_e32 v177, 11, v177
	v_lshlrev_b32_e32 v177, 2, v177
	v_add_u32_e32 v178, 6, v165
	v_min_u32_e32 v178, 11, v178
	v_lshlrev_b32_e32 v178, 2, v178
	v_add_u32_e32 v179, 7, v165
	v_min_u32_e32 v179, 11, v179
	v_lshlrev_b32_e32 v179, 2, v179
	v_add_u32_e32 v180, 0, v166
	v_min_u32_e32 v180, 11, v180
	v_lshlrev_b32_e32 v180, 2, v180
	v_add_u32_e32 v181, 1, v166
	v_min_u32_e32 v181, 11, v181
	v_lshlrev_b32_e32 v181, 2, v181
	v_add_u32_e32 v182, 2, v166
	v_min_u32_e32 v182, 11, v182
	v_lshlrev_b32_e32 v182, 2, v182
	v_add_u32_e32 v183, 3, v166
	v_min_u32_e32 v183, 11, v183
	v_lshlrev_b32_e32 v183, 2, v183
	v_add_u32_e32 v184, 4, v166
	v_min_u32_e32 v184, 11, v184
	v_lshlrev_b32_e32 v184, 2, v184
	v_add_u32_e32 v185, 5, v166
	v_min_u32_e32 v185, 11, v185
	v_lshlrev_b32_e32 v185, 2, v185
	v_add_u32_e32 v186, 6, v166
	v_min_u32_e32 v186, 11, v186
	v_lshlrev_b32_e32 v186, 2, v186
	v_add_u32_e32 v187, 7, v166
	v_min_u32_e32 v187, 11, v187
	v_lshlrev_b32_e32 v187, 2, v187
	global_load_dwordx4 v[100:103], v240, s[18:19] offset:0 sc1 nt
	global_load_dwordx4 v[104:107], v240, s[18:19] offset:2048 sc1 nt
	global_load_dwordx4 v[132:135], v240, s[20:21] offset:0 sc1 nt
	global_load_dwordx4 v[136:139], v240, s[20:21] offset:2048 sc1 nt
	global_load_dwordx4 v[108:111], v241, s[18:19] offset:0 sc1 nt
	global_load_dwordx4 v[112:115], v241, s[18:19] offset:2048 sc1 nt
	global_load_dwordx4 v[140:143], v241, s[20:21] offset:0 sc1 nt
	global_load_dwordx4 v[144:147], v241, s[20:21] offset:2048 sc1 nt
	global_load_dwordx4 v[116:119], v242, s[18:19] offset:0 sc1 nt
	global_load_dwordx4 v[120:123], v242, s[18:19] offset:2048 sc1 nt
	global_load_dwordx4 v[148:151], v242, s[20:21] offset:0 sc1 nt
	global_load_dwordx4 v[152:155], v242, s[20:21] offset:2048 sc1 nt
	global_load_dwordx4 v[124:127], v243, s[18:19] offset:0 sc1 nt
	global_load_dwordx4 v[128:131], v243, s[18:19] offset:2048 sc1 nt
	global_load_dwordx4 v[156:159], v243, s[20:21] offset:0 sc1 nt
	global_load_dwordx4 v[160:163], v243, s[20:21] offset:2048 sc1 nt
	s_cmp_eq_u32 s15, 7
	s_cselect_b32 s22, 0, 0x20000
	s_add_u32 s84, s18, s22
	s_addc_u32 s85, s19, 0
	s_add_u32 s86, s18, s22
	s_addc_u32 s87, s19, 0
	s_add_u32 s86, s86, 0x1000
	s_addc_u32 s87, s87, 0
	s_add_u32 s88, s20, s22
	s_addc_u32 s89, s21, 0
	s_add_u32 s90, s20, s22
	s_addc_u32 s91, s21, 0
	s_add_u32 s90, s90, 0x1000
	s_addc_u32 s91, s91, 0
	s_waitcnt lgkmcnt(0)
	v_writelane_b32 v171, s40, 0
	v_writelane_b32 v171, s41, 1
	v_writelane_b32 v171, s42, 2
	v_writelane_b32 v171, s43, 3
	v_writelane_b32 v171, s44, 4
	v_writelane_b32 v171, s45, 5
	v_writelane_b32 v171, s46, 6
	v_writelane_b32 v171, s47, 7
	v_writelane_b32 v171, s48, 8
	v_writelane_b32 v171, s49, 9
	v_writelane_b32 v171, s50, 10
	v_writelane_b32 v171, 0, 11
	v_fma_mixlo_f16 v171, v171, s51, 0
	ds_bpermute_b32 v188, v172, v171
	ds_bpermute_b32 v189, v173, v171
	ds_bpermute_b32 v190, v174, v171
	ds_bpermute_b32 v191, v175, v171
	ds_bpermute_b32 v192, v176, v171
	ds_bpermute_b32 v193, v177, v171
	ds_bpermute_b32 v194, v178, v171
	ds_bpermute_b32 v195, v179, v171
	v_mov_b32_e32 v229, 0x44800000
	v_fma_mixlo_f16 v228, s40, v229, 0
	v_cvt_f32_f16_e32 v228, v228
	v_cvt_f64_f32_e32 v[212:213], v228
	v_add_f64 v[212:213], v[212:213], 0
	v_fma_mixlo_f16 v228, s41, v229, 0
	v_cvt_f32_f16_e32 v228, v228
	v_cvt_f64_f32_e32 v[214:215], v228
	v_add_f64 v[212:213], v[212:213], v[214:215]
	v_fma_mixlo_f16 v228, s42, v229, 0
	v_cvt_f32_f16_e32 v228, v228
	v_cvt_f64_f32_e32 v[214:215], v228
	v_add_f64 v[212:213], v[212:213], v[214:215]
	v_fma_mixlo_f16 v228, s43, v229, 0
	v_cvt_f32_f16_e32 v228, v228
	v_cvt_f64_f32_e32 v[214:215], v228
	v_add_f64 v[212:213], v[212:213], v[214:215]
	v_fma_mixlo_f16 v228, s44, v229, 0
	v_cvt_f32_f16_e32 v228, v228
	v_cvt_f64_f32_e32 v[214:215], v228
	v_add_f64 v[212:213], v[212:213], v[214:215]
	v_fma_mixlo_f16 v228, s45, v229, 0
	v_cvt_f32_f16_e32 v228, v228
	v_cvt_f64_f32_e32 v[214:215], v228
	v_add_f64 v[212:213], v[212:213], v[214:215]
	v_fma_mixlo_f16 v228, s46, v229, 0
	v_cvt_f32_f16_e32 v228, v228
	v_cvt_f64_f32_e32 v[214:215], v228
	v_add_f64 v[212:213], v[212:213], v[214:215]
	v_fma_mixlo_f16 v228, s47, v229, 0
	v_cvt_f32_f16_e32 v228, v228
	v_cvt_f64_f32_e32 v[214:215], v228
	v_add_f64 v[212:213], v[212:213], v[214:215]
	v_fma_mixlo_f16 v228, s48, v229, 0
	v_cvt_f32_f16_e32 v228, v228
	v_cvt_f64_f32_e32 v[214:215], v228
	v_add_f64 v[212:213], v[212:213], v[214:215]
	v_fma_mixlo_f16 v228, s49, v229, 0
	v_cvt_f32_f16_e32 v228, v228
	v_cvt_f64_f32_e32 v[214:215], v228
	v_add_f64 v[212:213], v[212:213], v[214:215]
	v_fma_mixlo_f16 v228, s50, v229, 0
	v_cvt_f32_f16_e32 v228, v228
	v_cvt_f64_f32_e32 v[214:215], v228
	v_add_f64 v[212:213], v[212:213], v[214:215]
	s_waitcnt lgkmcnt(7)
	ds_bpermute_b32 v196, v180, v171
	ds_bpermute_b32 v197, v181, v171
	ds_bpermute_b32 v198, v182, v171
	ds_bpermute_b32 v199, v183, v171
	ds_bpermute_b32 v200, v184, v171
	ds_bpermute_b32 v201, v185, v171
	ds_bpermute_b32 v202, v186, v171
	ds_bpermute_b32 v203, v187, v171
	v_mul_f64 v[212:213], v[212:213], v[212:213]
	v_mul_f64 v[216:217], v[212:213], 0.5
	v_add_f64 v[218:219], v[216:217], v[216:217]
	s_mov_b32 s36, 0xeb1c432d
	s_mov_b32 s37, 0x3f1a36e2
	v_mul_f64 v[220:221], v[212:213], s[36:37]
	v_mul_f64 v[222:223], v[216:217], v[218:219]
	v_fmac_f64_e32 v[222:223], v[212:213], v[220:221]
	v_add_f64 v[224:225], v[212:213], v[212:213]
	s_mov_b32 s36, 0x487fcb92
	s_mov_b32 s37, 0x3f4d7dbf
	v_mul_f64 v[226:227], v[212:213], s[36:37]
	v_cvt_f32_f64_e32 v0, v[226:227]
	v_mov_b32_e32 v1, v0
	v_mov_b32_e32 v2, v0
	v_mov_b32_e32 v3, v0
	v_cvt_f32_f64_e32 v10, v[218:219]
	v_cvt_f32_f64_e32 v11, v[222:223]
	v_cvt_f32_f64_e32 v12, v[212:213]
	v_cvt_f32_f64_e32 v13, v[224:225]
	v_mul_f64 v[226:227], v[212:213], v[226:227]
	v_cvt_f32_f64_e32 v14, v[226:227]
	v_lshlrev_b32_e32 v167, 2, v164
	s_cmp_eq_u32 s12, 0
	s_cselect_b32 s23, 6, 64
	v_add_u32_e32 v168, 0, v167
	v_cmp_gt_u32_e32 vcc, s23, v168
	s_nop 1
	v_cndmask_b32_e64 v15, 0, 1.0, vcc
	v_add_u32_e32 v168, 1, v167
	v_cmp_gt_u32_e32 vcc, s23, v168
	s_nop 1
	v_cndmask_b32_e64 v16, 0, 1.0, vcc
	v_add_u32_e32 v168, 2, v167
	v_cmp_gt_u32_e32 vcc, s23, v168
	s_nop 1
	v_cndmask_b32_e64 v17, 0, 1.0, vcc
	v_add_u32_e32 v168, 3, v167
	v_cmp_gt_u32_e32 vcc, s23, v168
	s_nop 1
	v_cndmask_b32_e64 v18, 0, 1.0, vcc
	v_and_b32_e32 v167, 31, v8
	v_lshlrev_b32_e32 v167, 4, v167
	s_lshl_b32 s24, s12, 11
	s_add_i32 s25, s12, 7
	s_and_b32 s25, s25, 7
	s_lshl_b32 s26, s25, 11
	v_or_b32_e32 v4, s24, v167
	v_or_b32_e32 v5, s26, v167
	s_lshl_b32 s28, s25, 2
	s_add_u32 s28, s28, 0x10000
	v_mov_b32_e32 v7, s28
	v_mov_b32_e32 v19, 0
	v_mov_b32_e32 v20, 0
	v_mov_b32_e32 v21, 0
	v_mov_b32_e32 v22, 0
	s_waitcnt lgkmcnt(0)
	v_cmp_lt_u32_e64 s[32:33], 31, v8
	v_cmp_gt_u32_e64 s[34:35], 32, v8
	v_pack_b32_f16 v24, v188, v189
	v_pack_b32_f16 v25, v190, v191
	v_pack_b32_f16 v26, v192, v193
	v_pack_b32_f16 v27, v194, v195
	v_pack_b32_f16 v167, v196, v197
	v_cndmask_b32_e64 v28, 0, v167, s[32:33]
	v_cndmask_b32_e64 v32, 0, v167, s[34:35]
	v_pack_b32_f16 v167, v198, v199
	v_cndmask_b32_e64 v29, 0, v167, s[32:33]
	v_cndmask_b32_e64 v33, 0, v167, s[34:35]
	v_pack_b32_f16 v167, v200, v201
	v_cndmask_b32_e64 v30, 0, v167, s[32:33]
	v_cndmask_b32_e64 v34, 0, v167, s[34:35]
	v_pack_b32_f16 v167, v202, v203
	v_cndmask_b32_e64 v31, 0, v167, s[32:33]
	v_cndmask_b32_e64 v35, 0, v167, s[34:35]
	s_waitcnt lgkmcnt(0)
	s_cmp_lt_u32 s12, 4
	s_cbranch_scc1 .Lq_noprio
	s_setprio 1

.Lq_spin_0:
	s_nop 7
	ds_read_b32 v9, v7 offset:0
	s_waitcnt lgkmcnt(0)
	v_cmp_eq_u32_e32 vcc, 0, v9
	s_cbranch_vccnz .Lq_spin_0

.Lq_spin_1:
	s_nop 7
	ds_read_b32 v9, v7 offset:32
	s_waitcnt lgkmcnt(0)
	v_cmp_eq_u32_e32 vcc, 0, v9
	s_cbranch_vccnz .Lq_spin_1

.Lq_spin_2:
	s_nop 7
	ds_read_b32 v9, v7 offset:64
	s_waitcnt lgkmcnt(0)
	v_cmp_eq_u32_e32 vcc, 0, v9
	s_cbranch_vccnz .Lq_spin_2

.Lq_spin_3:
	s_nop 7
	ds_read_b32 v9, v7 offset:96
	s_waitcnt lgkmcnt(0)
	v_cmp_eq_u32_e32 vcc, 0, v9
	s_cbranch_vccnz .Lq_spin_3
